# first own k-step prelude (k+4 weight loads, next-node layer-0 address) hoisted into layer 0
# baseline (speedup 1.0000x reference)
.LBB1_4:
	s_and_saveexec_b64 s[8:9], s[2:3]
	v_perm_b32 v5, v1, v102, s23
	v_perm_b32 v9, v121, v103, s23
	v_perm_b32 v17, v144, v115, s23
	v_perm_b32 v29, v145, v116, s23
	s_or_b64 exec, exec, s[8:9]
	v_mfma_f32_16x16x32_f16 v[164:167], v[30:33], v[2:5], 0
	v_mfma_f32_16x16x32_f16 v[180:183], v[22:25], v[2:5], 0
	s_cmp_lg_u32 s22, 0x818000
	v_mfma_f32_16x16x32_f16 v[168:171], v[30:33], v[6:9], 0
	v_mfma_f32_16x16x32_f16 v[184:187], v[22:25], v[6:9], 0
	s_cselect_b32 s9, s11, 15
	v_mfma_f32_16x16x32_f16 v[172:175], v[30:33], v[14:17], 0
	v_mfma_f32_16x16x32_f16 v[188:191], v[22:25], v[14:17], 0
	v_mfma_f32_16x16x32_f16 v[176:179], v[30:33], v[26:29], 0
	v_mfma_f32_16x16x32_f16 v[116:119], v[22:25], v[26:29], 0
	s_lshl_b32 s20, s9, 7
	v_lshl_add_u64 v[0:1], s[20:21], 3, v[132:133]
	s_add_i32 s25, s22, s34
	s_lshl_b32 s8, s9, 8
	buffer_load_dwordx4 v[192:195], v147, s[16:19], s25 offen
	buffer_load_dwordx4 v[196:199], v148, s[16:19], s25 offen
	buffer_load_dwordx4 v[200:203], v149, s[16:19], s25 offen
	buffer_load_dwordx4 v[204:207], v150, s[16:19], s25 offen
	v_mfma_f32_16x16x32_f16 v[208:211], v[18:21], v[2:5], 0
	v_cvt_pk_f16_f32 v122, v164, v165
	v_cvt_pk_f16_f32 v123, v166, v167
	v_pk_max_f16 v122, v122, 0
	v_pk_max_f16 v123, v123, 0
	v_cvt_pk_f16_f32 v124, v180, v181
	v_cvt_pk_f16_f32 v125, v182, v183
	v_pk_max_f16 v124, v124, 0
	v_pk_max_f16 v125, v125, 0
	ds_write_b128 v107, v[122:125]
	v_mfma_f32_16x16x32_f16 v[224:227], v[10:13], v[2:5], 0
	v_cvt_pk_f16_f32 v126, v168, v169
	v_cvt_pk_f16_f32 v127, v170, v171
	v_pk_max_f16 v126, v126, 0
	v_pk_max_f16 v127, v127, 0
	v_cvt_pk_f16_f32 v128, v184, v185
	v_cvt_pk_f16_f32 v129, v186, v187
	v_pk_max_f16 v128, v128, 0
	v_pk_max_f16 v129, v129, 0
	ds_write_b128 v107, v[126:129] offset:16384
	v_mfma_f32_16x16x32_f16 v[212:215], v[18:21], v[6:9], 0
	v_cvt_pk_f16_f32 v134, v172, v173
	v_cvt_pk_f16_f32 v135, v174, v175
	v_pk_max_f16 v134, v134, 0
	v_pk_max_f16 v135, v135, 0
	v_cvt_pk_f16_f32 v136, v188, v189
	v_cvt_pk_f16_f32 v137, v190, v191
	v_pk_max_f16 v136, v136, 0
	v_pk_max_f16 v137, v137, 0
	ds_write_b128 v107, v[134:137] offset:32768
	v_mfma_f32_16x16x32_f16 v[228:231], v[10:13], v[6:9], 0
	v_cvt_pk_f16_f32 v138, v176, v177
	v_cvt_pk_f16_f32 v139, v178, v179
	v_pk_max_f16 v138, v138, 0
	v_pk_max_f16 v139, v139, 0
	v_cvt_pk_f16_f32 v140, v116, v117
	v_cvt_pk_f16_f32 v141, v118, v119
	v_pk_max_f16 v140, v140, 0
	v_pk_max_f16 v141, v141, 0
	ds_write_b128 v107, v[138:141] offset:49152
	v_mfma_f32_16x16x32_f16 v[216:219], v[18:21], v[14:17], 0
	v_mfma_f32_16x16x32_f16 v[232:235], v[10:13], v[14:17], 0
	v_mfma_f32_16x16x32_f16 v[220:223], v[18:21], v[26:29], 0
	v_mfma_f32_16x16x32_f16 v[236:239], v[10:13], v[26:29], 0
	v_add_u32_e32 v111, s64, v111
	v_add_u32_e32 v98, s65, v98
	s_waitcnt vmcnt(19)
	v_mfma_f32_16x16x32_f16 v[164:167], v[58:61], v[122:125], v[240:243]
	v_cvt_pk_f16_f32 v142, v208, v209
	v_cvt_pk_f16_f32 v143, v210, v211
	v_mfma_f32_16x16x32_f16 v[168:171], v[58:61], v[126:129], v[240:243]
	v_pk_max_f16 v142, v142, 0
	v_pk_max_f16 v143, v143, 0
	v_mfma_f32_16x16x32_f16 v[172:175], v[58:61], v[134:137], v[240:243]
	v_cvt_pk_f16_f32 v144, v224, v225
	v_cvt_pk_f16_f32 v145, v226, v227
	v_mfma_f32_16x16x32_f16 v[10:13], v[58:61], v[138:141], v[240:243]
	v_pk_max_f16 v144, v144, 0
	v_pk_max_f16 v145, v145, 0
	ds_write_b128 v108, v[142:145]
	s_waitcnt vmcnt(18)
	v_mfma_f32_16x16x32_f16 v[58:61], v[54:57], v[122:125], v[244:247]
	v_cvt_pk_f16_f32 v152, v212, v213
	v_cvt_pk_f16_f32 v153, v214, v215
	v_mfma_f32_16x16x32_f16 v[176:179], v[54:57], v[126:129], v[244:247]
	v_pk_max_f16 v152, v152, 0
	v_pk_max_f16 v153, v153, 0
	v_mfma_f32_16x16x32_f16 v[180:183], v[54:57], v[134:137], v[244:247]
	v_cvt_pk_f16_f32 v154, v228, v229
	v_cvt_pk_f16_f32 v155, v230, v231
	v_mfma_f32_16x16x32_f16 v[18:21], v[54:57], v[138:141], v[244:247]
	v_pk_max_f16 v154, v154, 0
	v_pk_max_f16 v155, v155, 0
	ds_write_b128 v108, v[152:155] offset:16384
	s_waitcnt vmcnt(17)
	v_mfma_f32_16x16x32_f16 v[54:57], v[50:53], v[122:125], v[248:251]
	v_cvt_pk_f16_f32 v156, v216, v217
	v_cvt_pk_f16_f32 v157, v218, v219
	v_mfma_f32_16x16x32_f16 v[184:187], v[50:53], v[126:129], v[248:251]
	v_pk_max_f16 v156, v156, 0
	v_pk_max_f16 v157, v157, 0
	v_mfma_f32_16x16x32_f16 v[188:191], v[50:53], v[134:137], v[248:251]
	v_cvt_pk_f16_f32 v158, v232, v233
	v_cvt_pk_f16_f32 v159, v234, v235
	v_mfma_f32_16x16x32_f16 v[22:25], v[50:53], v[138:141], v[248:251]
	v_pk_max_f16 v158, v158, 0
	v_pk_max_f16 v159, v159, 0
	ds_write_b128 v108, v[156:159] offset:32768
	s_waitcnt vmcnt(16)
	v_mfma_f32_16x16x32_f16 v[50:53], v[38:41], v[122:125], v[252:255]
	v_cvt_pk_f16_f32 v160, v220, v221
	v_cvt_pk_f16_f32 v161, v222, v223
	v_mfma_f32_16x16x32_f16 v[122:125], v[38:41], v[126:129], v[252:255]
	v_pk_max_f16 v160, v160, 0
	v_pk_max_f16 v161, v161, 0
	v_mfma_f32_16x16x32_f16 v[126:129], v[38:41], v[134:137], v[252:255]
	v_cvt_pk_f16_f32 v162, v236, v237
	v_cvt_pk_f16_f32 v163, v238, v239
	v_mfma_f32_16x16x32_f16 v[38:41], v[38:41], v[138:141], v[252:255]
	v_pk_max_f16 v162, v162, 0
	v_pk_max_f16 v163, v163, 0
	ds_write_b128 v108, v[160:163] offset:49152
	s_add_i32 s9, s22, s35
	s_waitcnt vmcnt(15)
	v_mfma_f32_16x16x32_f16 v[164:167], v[94:97], v[142:145], v[164:167]
	v_mfma_f32_16x16x32_f16 v[168:171], v[94:97], v[152:155], v[168:171]
	s_waitcnt vmcnt(14)
	v_mfma_f32_16x16x32_f16 v[58:61], v[90:93], v[142:145], v[58:61]
	v_mfma_f32_16x16x32_f16 v[176:179], v[90:93], v[152:155], v[176:179]
	s_waitcnt vmcnt(13)
	v_mfma_f32_16x16x32_f16 v[54:57], v[78:81], v[142:145], v[54:57]
	v_mfma_f32_16x16x32_f16 v[184:187], v[78:81], v[152:155], v[184:187]
	s_waitcnt vmcnt(12)
	v_mfma_f32_16x16x32_f16 v[50:53], v[34:37], v[142:145], v[50:53]
	buffer_load_dwordx4 v[140:143], v147, s[16:19], s9 offen
	buffer_load_dwordx4 v[220:223], v148, s[16:19], s9 offen
	v_mfma_f32_16x16x32_f16 v[122:125], v[34:37], v[152:155], v[122:125]
	buffer_load_dwordx4 v[152:155], v149, s[16:19], s9 offen
	buffer_load_dwordx4 v[224:227], v150, s[16:19], s9 offen
	s_mov_b32 s9, s21
	s_waitcnt lgkmcnt(0)
	s_barrier
	v_add_u32_e32 v99, s66, v99
	ds_read_b128 v[136:139], v99
	ds_read_b128 v[208:211], v99 offset:16384
	ds_read_b128 v[212:215], v99 offset:32768
	ds_read_b128 v[216:219], v99 offset:49152
	v_mfma_f32_16x16x32_f16 v[172:175], v[94:97], v[156:159], v[172:175]
	v_mfma_f32_16x16x32_f16 v[94:97], v[94:97], v[160:163], v[10:13]
	s_nop 2
	v_lshl_add_u64 v[10:11], s[8:9], 4, v[130:131]
	v_mfma_f32_16x16x32_f16 v[180:183], v[90:93], v[156:159], v[180:183]
	v_mfma_f32_16x16x32_f16 v[90:93], v[90:93], v[160:163], v[18:21]
	v_mfma_f32_16x16x32_f16 v[188:191], v[78:81], v[156:159], v[188:191]
	v_mfma_f32_16x16x32_f16 v[78:81], v[78:81], v[160:163], v[22:25]
	global_load_dwordx4 v[30:33], v[10:11], off
	s_nop 1
	global_load_dwordx4 v[22:25], v[10:11], off offset:1024
	global_load_dwordx4 v[18:21], v[10:11], off offset:2048
	s_nop 0
	global_load_dwordx4 v[10:13], v[10:11], off offset:3072
	s_nop 0
	global_load_dwordx2 v[134:135], v[0:1], off
	v_mfma_f32_16x16x32_f16 v[126:129], v[34:37], v[156:159], v[126:129]
	v_mfma_f32_16x16x32_f16 v[34:37], v[34:37], v[160:163], v[38:41]
	s_nop 2
	v_add_u32_e32 v100, s67, v100
	ds_read_b128 v[38:41], v100
	ds_read_b128 v[156:159], v100 offset:16384
	ds_read_b128 v[160:163], v100 offset:32768
	ds_read_b128 v[228:231], v100 offset:49152
	s_add_i32 s8, s22, s36
	s_waitcnt vmcnt(20) lgkmcnt(7)
	v_mfma_f32_16x16x32_f16 v[164:167], v[82:85], v[136:139], v[164:167]
	s_waitcnt lgkmcnt(6)
	v_mfma_f32_16x16x32_f16 v[168:171], v[82:85], v[208:211], v[168:171]
	s_waitcnt lgkmcnt(5)
	v_mfma_f32_16x16x32_f16 v[172:175], v[82:85], v[212:215], v[172:175]
	s_waitcnt lgkmcnt(4)
	v_mfma_f32_16x16x32_f16 v[82:85], v[82:85], v[216:219], v[94:97]
	s_waitcnt vmcnt(19)
	v_mfma_f32_16x16x32_f16 v[58:61], v[70:73], v[136:139], v[58:61]
	v_mfma_f32_16x16x32_f16 v[94:97], v[70:73], v[208:211], v[176:179]
	v_mfma_f32_16x16x32_f16 v[176:179], v[70:73], v[212:215], v[180:183]
	v_mfma_f32_16x16x32_f16 v[70:73], v[70:73], v[216:219], v[90:93]
	s_waitcnt vmcnt(18)
	v_mfma_f32_16x16x32_f16 v[54:57], v[62:65], v[136:139], v[54:57]
	v_mfma_f32_16x16x32_f16 v[90:93], v[62:65], v[208:211], v[184:187]
	v_mfma_f32_16x16x32_f16 v[180:183], v[62:65], v[212:215], v[188:191]
	v_mfma_f32_16x16x32_f16 v[62:65], v[62:65], v[216:219], v[78:81]
	s_waitcnt vmcnt(17)
	v_mfma_f32_16x16x32_f16 v[50:53], v[42:45], v[136:139], v[50:53]
	v_mfma_f32_16x16x32_f16 v[78:81], v[42:45], v[208:211], v[122:125]
	v_mfma_f32_16x16x32_f16 v[122:125], v[42:45], v[212:215], v[126:129]
	s_nop 2
	buffer_load_dwordx4 v[126:129], v147, s[16:19], s8 offen
	buffer_load_dwordx4 v[136:139], v148, s[16:19], s8 offen
	buffer_load_dwordx4 v[184:187], v149, s[16:19], s8 offen
	buffer_load_dwordx4 v[188:191], v150, s[16:19], s8 offen
	v_mfma_f32_16x16x32_f16 v[34:37], v[42:45], v[216:219], v[34:37]
	v_add_u32_e32 v111, s68, v111
	ds_read_b128 v[42:45], v111
	ds_read_b128 v[208:211], v111 offset:16384
	ds_read_b128 v[212:215], v111 offset:32768
	ds_read_b128 v[216:219], v111 offset:49152
	s_add_i32 s8, s22, s37
	s_waitcnt vmcnt(20) lgkmcnt(7)
	v_mfma_f32_16x16x32_f16 v[164:167], v[86:89], v[38:41], v[164:167]
	s_waitcnt lgkmcnt(6)
	v_mfma_f32_16x16x32_f16 v[168:171], v[86:89], v[156:159], v[168:171]
	s_waitcnt lgkmcnt(5)
	v_mfma_f32_16x16x32_f16 v[172:175], v[86:89], v[160:163], v[172:175]
	s_waitcnt lgkmcnt(4)
	v_mfma_f32_16x16x32_f16 v[82:85], v[86:89], v[228:231], v[82:85]
	s_waitcnt vmcnt(19)
	v_mfma_f32_16x16x32_f16 v[58:61], v[74:77], v[38:41], v[58:61]
	v_mfma_f32_16x16x32_f16 v[86:89], v[74:77], v[156:159], v[94:97]
	v_mfma_f32_16x16x32_f16 v[94:97], v[74:77], v[160:163], v[176:179]
	v_mfma_f32_16x16x32_f16 v[70:73], v[74:77], v[228:231], v[70:73]
	s_waitcnt vmcnt(18)
	v_mfma_f32_16x16x32_f16 v[54:57], v[66:69], v[38:41], v[54:57]
	v_mfma_f32_16x16x32_f16 v[74:77], v[66:69], v[156:159], v[90:93]
	v_mfma_f32_16x16x32_f16 v[90:93], v[66:69], v[160:163], v[180:183]
	v_mfma_f32_16x16x32_f16 v[62:65], v[66:69], v[228:231], v[62:65]
	s_waitcnt vmcnt(17)
	v_mfma_f32_16x16x32_f16 v[38:41], v[46:49], v[38:41], v[50:53]
	v_mfma_f32_16x16x32_f16 v[50:53], v[46:49], v[156:159], v[78:81]
	v_mfma_f32_16x16x32_f16 v[66:69], v[46:49], v[160:163], v[122:125]
	s_nop 1
	buffer_load_dwordx4 v[78:81], v147, s[16:19], s8 offen
	buffer_load_dwordx4 v[122:125], v148, s[16:19], s8 offen
	buffer_load_dwordx4 v[156:159], v149, s[16:19], s8 offen
	buffer_load_dwordx4 v[160:163], v150, s[16:19], s8 offen
	v_mfma_f32_16x16x32_f16 v[34:37], v[46:49], v[228:231], v[34:37]
	v_add_u32_e32 v98, s69, v98
	ds_read_b128 v[46:49], v98
	ds_read_b128 v[176:179], v98 offset:16384
	ds_read_b128 v[180:183], v98 offset:32768
	ds_read_b128 v[228:231], v98 offset:49152
	s_add_i32 s8, s22, s38
	s_waitcnt vmcnt(20) lgkmcnt(7)
	v_mfma_f32_16x16x32_f16 v[164:167], v[192:195], v[42:45], v[164:167]
	s_waitcnt lgkmcnt(6)
	v_mfma_f32_16x16x32_f16 v[168:171], v[192:195], v[208:211], v[168:171]
	s_waitcnt lgkmcnt(5)
	v_mfma_f32_16x16x32_f16 v[172:175], v[192:195], v[212:215], v[172:175]
	s_waitcnt lgkmcnt(4)
	v_mfma_f32_16x16x32_f16 v[82:85], v[192:195], v[216:219], v[82:85]
	s_waitcnt vmcnt(19)
	v_mfma_f32_16x16x32_f16 v[58:61], v[196:199], v[42:45], v[58:61]
	v_mfma_f32_16x16x32_f16 v[86:89], v[196:199], v[208:211], v[86:89]
	v_mfma_f32_16x16x32_f16 v[94:97], v[196:199], v[212:215], v[94:97]
	v_mfma_f32_16x16x32_f16 v[70:73], v[196:199], v[216:219], v[70:73]
	s_waitcnt vmcnt(18)
	v_mfma_f32_16x16x32_f16 v[54:57], v[200:203], v[42:45], v[54:57]
	v_mfma_f32_16x16x32_f16 v[74:77], v[200:203], v[208:211], v[74:77]
	v_mfma_f32_16x16x32_f16 v[90:93], v[200:203], v[212:215], v[90:93]
	v_mfma_f32_16x16x32_f16 v[62:65], v[200:203], v[216:219], v[62:65]
	s_waitcnt vmcnt(17)
	v_mfma_f32_16x16x32_f16 v[38:41], v[204:207], v[42:45], v[38:41]
	v_mfma_f32_16x16x32_f16 v[42:45], v[204:207], v[208:211], v[50:53]
	v_mfma_f32_16x16x32_f16 v[50:53], v[204:207], v[212:215], v[66:69]
	s_nop 2
	buffer_load_dwordx4 v[66:69], v147, s[16:19], s8 offen
	buffer_load_dwordx4 v[192:195], v148, s[16:19], s8 offen
	buffer_load_dwordx4 v[196:199], v149, s[16:19], s8 offen
	buffer_load_dwordx4 v[200:203], v150, s[16:19], s8 offen
	v_mfma_f32_16x16x32_f16 v[34:37], v[204:207], v[216:219], v[34:37]
	v_add_u32_e32 v99, s70, v99
	ds_read_b128 v[204:207], v99
	ds_read_b128 v[208:211], v99 offset:16384
	ds_read_b128 v[212:215], v99 offset:32768
	ds_read_b128 v[216:219], v99 offset:49152
	s_add_i32 s8, s22, s39
	s_waitcnt vmcnt(20) lgkmcnt(7)
	v_mfma_f32_16x16x32_f16 v[164:167], v[140:143], v[46:49], v[164:167]
	s_waitcnt lgkmcnt(6)
	v_mfma_f32_16x16x32_f16 v[168:171], v[140:143], v[176:179], v[168:171]
	s_waitcnt lgkmcnt(5)
	v_mfma_f32_16x16x32_f16 v[172:175], v[140:143], v[180:183], v[172:175]
	s_waitcnt lgkmcnt(4)
	v_mfma_f32_16x16x32_f16 v[82:85], v[140:143], v[228:231], v[82:85]
	s_waitcnt vmcnt(19)
	v_mfma_f32_16x16x32_f16 v[58:61], v[220:223], v[46:49], v[58:61]
	v_mfma_f32_16x16x32_f16 v[86:89], v[220:223], v[176:179], v[86:89]
	s_waitcnt vmcnt(18)
	v_mfma_f32_16x16x32_f16 v[54:57], v[152:155], v[46:49], v[54:57]
	v_mfma_f32_16x16x32_f16 v[74:77], v[152:155], v[176:179], v[74:77]
	v_mfma_f32_16x16x32_f16 v[90:93], v[152:155], v[180:183], v[90:93]
	v_mfma_f32_16x16x32_f16 v[62:65], v[152:155], v[228:231], v[62:65]
	s_waitcnt vmcnt(17)
	v_mfma_f32_16x16x32_f16 v[38:41], v[224:227], v[46:49], v[38:41]
	v_mfma_f32_16x16x32_f16 v[42:45], v[224:227], v[176:179], v[42:45]
	v_mfma_f32_16x16x32_f16 v[46:49], v[224:227], v[180:183], v[50:53]
	s_nop 2
	buffer_load_dwordx4 v[50:53], v147, s[16:19], s8 offen
	buffer_load_dwordx4 v[140:143], v148, s[16:19], s8 offen
	buffer_load_dwordx4 v[152:155], v149, s[16:19], s8 offen
	buffer_load_dwordx4 v[176:179], v150, s[16:19], s8 offen
	v_mfma_f32_16x16x32_f16 v[94:97], v[220:223], v[180:183], v[94:97]
	v_mfma_f32_16x16x32_f16 v[70:73], v[220:223], v[228:231], v[70:73]
	v_mfma_f32_16x16x32_f16 v[34:37], v[224:227], v[228:231], v[34:37]
	v_add_u32_e32 v100, s71, v100
	ds_read_b128 v[180:183], v100
	ds_read_b128 v[220:223], v100 offset:16384
	ds_read_b128 v[224:227], v100 offset:32768
	ds_read_b128 v[228:231], v100 offset:49152
	s_add_i32 s8, s22, s40
	s_waitcnt vmcnt(15) lgkmcnt(7)
	v_mfma_f32_16x16x32_f16 v[164:167], v[126:129], v[204:207], v[164:167]
	s_waitcnt lgkmcnt(6)
	v_mfma_f32_16x16x32_f16 v[168:171], v[126:129], v[208:211], v[168:171]
	s_waitcnt lgkmcnt(5)
	v_mfma_f32_16x16x32_f16 v[172:175], v[126:129], v[212:215], v[172:175]
	s_waitcnt lgkmcnt(4)
	v_mfma_f32_16x16x32_f16 v[82:85], v[126:129], v[216:219], v[82:85]
	s_waitcnt vmcnt(14)
	v_mfma_f32_16x16x32_f16 v[58:61], v[136:139], v[204:207], v[58:61]
	v_mfma_f32_16x16x32_f16 v[86:89], v[136:139], v[208:211], v[86:89]
	v_mfma_f32_16x16x32_f16 v[94:97], v[136:139], v[212:215], v[94:97]
	v_mfma_f32_16x16x32_f16 v[70:73], v[136:139], v[216:219], v[70:73]
	s_waitcnt vmcnt(13)
	v_mfma_f32_16x16x32_f16 v[54:57], v[184:187], v[204:207], v[54:57]
	v_mfma_f32_16x16x32_f16 v[74:77], v[184:187], v[208:211], v[74:77]
	v_mfma_f32_16x16x32_f16 v[90:93], v[184:187], v[212:215], v[90:93]
	v_mfma_f32_16x16x32_f16 v[62:65], v[184:187], v[216:219], v[62:65]
	s_waitcnt vmcnt(12)
	v_mfma_f32_16x16x32_f16 v[38:41], v[188:191], v[204:207], v[38:41]
	buffer_load_dwordx4 v[126:129], v147, s[16:19], s8 offen
	buffer_load_dwordx4 v[136:139], v148, s[16:19], s8 offen
	buffer_load_dwordx4 v[184:187], v149, s[16:19], s8 offen
	buffer_load_dwordx4 v[204:207], v150, s[16:19], s8 offen
	v_mfma_f32_16x16x32_f16 v[42:45], v[188:191], v[208:211], v[42:45]
	v_mfma_f32_16x16x32_f16 v[46:49], v[188:191], v[212:215], v[46:49]
	v_mfma_f32_16x16x32_f16 v[34:37], v[188:191], v[216:219], v[34:37]
	v_add_u32_e32 v111, s72, v111
	ds_read_b128 v[188:191], v111
	ds_read_b128 v[208:211], v111 offset:16384
	ds_read_b128 v[212:215], v111 offset:32768
	ds_read_b128 v[216:219], v111 offset:49152
	s_add_i32 s8, s22, s41
	s_waitcnt vmcnt(15) lgkmcnt(7)
	v_mfma_f32_16x16x32_f16 v[164:167], v[78:81], v[180:183], v[164:167]
	s_waitcnt lgkmcnt(6)
	v_mfma_f32_16x16x32_f16 v[168:171], v[78:81], v[220:223], v[168:171]
	s_waitcnt lgkmcnt(5)
	v_mfma_f32_16x16x32_f16 v[172:175], v[78:81], v[224:227], v[172:175]
	s_waitcnt lgkmcnt(4)
	v_mfma_f32_16x16x32_f16 v[78:81], v[78:81], v[228:231], v[82:85]
	s_waitcnt vmcnt(14)
	v_mfma_f32_16x16x32_f16 v[58:61], v[122:125], v[180:183], v[58:61]
	v_mfma_f32_16x16x32_f16 v[82:85], v[122:125], v[220:223], v[86:89]
	v_mfma_f32_16x16x32_f16 v[86:89], v[122:125], v[224:227], v[94:97]
	v_mfma_f32_16x16x32_f16 v[70:73], v[122:125], v[228:231], v[70:73]
	s_waitcnt vmcnt(13)
	v_mfma_f32_16x16x32_f16 v[54:57], v[156:159], v[180:183], v[54:57]
	v_mfma_f32_16x16x32_f16 v[74:77], v[156:159], v[220:223], v[74:77]
	v_mfma_f32_16x16x32_f16 v[90:93], v[156:159], v[224:227], v[90:93]
	v_mfma_f32_16x16x32_f16 v[62:65], v[156:159], v[228:231], v[62:65]
	s_waitcnt vmcnt(12)
	v_mfma_f32_16x16x32_f16 v[38:41], v[160:163], v[180:183], v[38:41]
	buffer_load_dwordx4 v[94:97], v147, s[16:19], s8 offen
	buffer_load_dwordx4 v[122:125], v148, s[16:19], s8 offen
	buffer_load_dwordx4 v[156:159], v149, s[16:19], s8 offen
	buffer_load_dwordx4 v[180:183], v150, s[16:19], s8 offen
	v_mfma_f32_16x16x32_f16 v[42:45], v[160:163], v[220:223], v[42:45]
	v_mfma_f32_16x16x32_f16 v[46:49], v[160:163], v[224:227], v[46:49]
	v_mfma_f32_16x16x32_f16 v[34:37], v[160:163], v[228:231], v[34:37]
	v_add_u32_e32 v98, s73, v98
	ds_read_b128 v[160:163], v98
	ds_read_b128 v[220:223], v98 offset:16384
	ds_read_b128 v[224:227], v98 offset:32768
	ds_read_b128 v[228:231], v98 offset:49152
	s_add_i32 s8, s22, s42
	s_waitcnt vmcnt(15) lgkmcnt(7)
	v_mfma_f32_16x16x32_f16 v[164:167], v[66:69], v[188:191], v[164:167]
	s_waitcnt lgkmcnt(6)
	v_mfma_f32_16x16x32_f16 v[168:171], v[66:69], v[208:211], v[168:171]
	s_waitcnt lgkmcnt(5)
	v_mfma_f32_16x16x32_f16 v[172:175], v[66:69], v[212:215], v[172:175]
	s_waitcnt lgkmcnt(4)
	v_mfma_f32_16x16x32_f16 v[66:69], v[66:69], v[216:219], v[78:81]
	s_waitcnt vmcnt(14)
	v_mfma_f32_16x16x32_f16 v[58:61], v[192:195], v[188:191], v[58:61]
	v_mfma_f32_16x16x32_f16 v[78:81], v[192:195], v[208:211], v[82:85]
	v_mfma_f32_16x16x32_f16 v[82:85], v[192:195], v[212:215], v[86:89]
	v_mfma_f32_16x16x32_f16 v[70:73], v[192:195], v[216:219], v[70:73]
	s_waitcnt vmcnt(13)
	v_mfma_f32_16x16x32_f16 v[54:57], v[196:199], v[188:191], v[54:57]
	v_mfma_f32_16x16x32_f16 v[74:77], v[196:199], v[208:211], v[74:77]
	v_mfma_f32_16x16x32_f16 v[86:89], v[196:199], v[212:215], v[90:93]
	v_mfma_f32_16x16x32_f16 v[62:65], v[196:199], v[216:219], v[62:65]
	s_waitcnt vmcnt(12)
	v_mfma_f32_16x16x32_f16 v[38:41], v[200:203], v[188:191], v[38:41]
	buffer_load_dwordx4 v[90:93], v147, s[16:19], s8 offen
	buffer_load_dwordx4 v[188:191], v148, s[16:19], s8 offen
	buffer_load_dwordx4 v[192:195], v149, s[16:19], s8 offen
	buffer_load_dwordx4 v[196:199], v150, s[16:19], s8 offen
	v_mfma_f32_16x16x32_f16 v[42:45], v[200:203], v[208:211], v[42:45]
	v_mfma_f32_16x16x32_f16 v[46:49], v[200:203], v[212:215], v[46:49]
	v_mfma_f32_16x16x32_f16 v[34:37], v[200:203], v[216:219], v[34:37]
	v_add_u32_e32 v99, s74, v99
	ds_read_b128 v[200:203], v99
	ds_read_b128 v[208:211], v99 offset:16384
	ds_read_b128 v[212:215], v99 offset:32768
	ds_read_b128 v[216:219], v99 offset:49152
	s_add_i32 s8, s22, s43
	s_waitcnt vmcnt(15) lgkmcnt(7)
	v_mfma_f32_16x16x32_f16 v[164:167], v[50:53], v[160:163], v[164:167]
	s_waitcnt lgkmcnt(6)
	v_mfma_f32_16x16x32_f16 v[168:171], v[50:53], v[220:223], v[168:171]
	s_waitcnt lgkmcnt(5)
	v_mfma_f32_16x16x32_f16 v[172:175], v[50:53], v[224:227], v[172:175]
	s_waitcnt lgkmcnt(4)
	v_mfma_f32_16x16x32_f16 v[50:53], v[50:53], v[228:231], v[66:69]
	s_waitcnt vmcnt(14)
	v_mfma_f32_16x16x32_f16 v[58:61], v[140:143], v[160:163], v[58:61]
	v_mfma_f32_16x16x32_f16 v[66:69], v[140:143], v[220:223], v[78:81]
	v_mfma_f32_16x16x32_f16 v[78:81], v[140:143], v[224:227], v[82:85]
	v_mfma_f32_16x16x32_f16 v[70:73], v[140:143], v[228:231], v[70:73]
	s_waitcnt vmcnt(13)
	v_mfma_f32_16x16x32_f16 v[54:57], v[152:155], v[160:163], v[54:57]
	v_mfma_f32_16x16x32_f16 v[74:77], v[152:155], v[220:223], v[74:77]
	v_mfma_f32_16x16x32_f16 v[82:85], v[152:155], v[224:227], v[86:89]
	v_mfma_f32_16x16x32_f16 v[62:65], v[152:155], v[228:231], v[62:65]
	s_waitcnt vmcnt(12)
	v_mfma_f32_16x16x32_f16 v[38:41], v[176:179], v[160:163], v[38:41]
	buffer_load_dwordx4 v[86:89], v147, s[16:19], s8 offen
	buffer_load_dwordx4 v[140:143], v148, s[16:19], s8 offen
	buffer_load_dwordx4 v[152:155], v149, s[16:19], s8 offen
	buffer_load_dwordx4 v[160:163], v150, s[16:19], s8 offen
	v_mfma_f32_16x16x32_f16 v[42:45], v[176:179], v[220:223], v[42:45]
	v_mfma_f32_16x16x32_f16 v[46:49], v[176:179], v[224:227], v[46:49]
	v_mfma_f32_16x16x32_f16 v[34:37], v[176:179], v[228:231], v[34:37]
	v_add_u32_e32 v100, s75, v100
	ds_read_b128 v[176:179], v100
	ds_read_b128 v[220:223], v100 offset:16384
	ds_read_b128 v[224:227], v100 offset:32768
	ds_read_b128 v[228:231], v100 offset:49152
	s_add_i32 s8, s22, s44
	s_waitcnt vmcnt(15) lgkmcnt(7)
	v_mfma_f32_16x16x32_f16 v[164:167], v[126:129], v[200:203], v[164:167]
	s_waitcnt lgkmcnt(6)
	v_mfma_f32_16x16x32_f16 v[168:171], v[126:129], v[208:211], v[168:171]
	s_waitcnt lgkmcnt(5)
	v_mfma_f32_16x16x32_f16 v[172:175], v[126:129], v[212:215], v[172:175]
	s_waitcnt lgkmcnt(4)
	v_mfma_f32_16x16x32_f16 v[50:53], v[126:129], v[216:219], v[50:53]
	s_waitcnt vmcnt(14)
	v_mfma_f32_16x16x32_f16 v[58:61], v[136:139], v[200:203], v[58:61]
	v_mfma_f32_16x16x32_f16 v[66:69], v[136:139], v[208:211], v[66:69]
	v_mfma_f32_16x16x32_f16 v[78:81], v[136:139], v[212:215], v[78:81]
	v_mfma_f32_16x16x32_f16 v[70:73], v[136:139], v[216:219], v[70:73]
	s_waitcnt vmcnt(13)
	v_mfma_f32_16x16x32_f16 v[54:57], v[184:187], v[200:203], v[54:57]
	v_mfma_f32_16x16x32_f16 v[74:77], v[184:187], v[208:211], v[74:77]
	v_mfma_f32_16x16x32_f16 v[82:85], v[184:187], v[212:215], v[82:85]
	v_mfma_f32_16x16x32_f16 v[62:65], v[184:187], v[216:219], v[62:65]
	s_waitcnt vmcnt(12)
	v_mfma_f32_16x16x32_f16 v[38:41], v[204:207], v[200:203], v[38:41]
	buffer_load_dwordx4 v[126:129], v147, s[16:19], s8 offen
	buffer_load_dwordx4 v[136:139], v148, s[16:19], s8 offen
	buffer_load_dwordx4 v[184:187], v149, s[16:19], s8 offen
	buffer_load_dwordx4 v[200:203], v150, s[16:19], s8 offen
	v_mfma_f32_16x16x32_f16 v[42:45], v[204:207], v[208:211], v[42:45]
	v_mfma_f32_16x16x32_f16 v[46:49], v[204:207], v[212:215], v[46:49]
	v_mfma_f32_16x16x32_f16 v[34:37], v[204:207], v[216:219], v[34:37]
	v_add_u32_e32 v111, s76, v111
	ds_read_b128 v[204:207], v111
	ds_read_b128 v[208:211], v111 offset:16384
	ds_read_b128 v[212:215], v111 offset:32768
	ds_read_b128 v[216:219], v111 offset:49152
	s_add_i32 s8, s22, s45
	s_waitcnt vmcnt(15) lgkmcnt(7)
	v_mfma_f32_16x16x32_f16 v[164:167], v[94:97], v[176:179], v[164:167]
	s_waitcnt lgkmcnt(6)
	v_mfma_f32_16x16x32_f16 v[168:171], v[94:97], v[220:223], v[168:171]
	s_waitcnt vmcnt(14)
	v_mfma_f32_16x16x32_f16 v[58:61], v[122:125], v[176:179], v[58:61]
	v_mfma_f32_16x16x32_f16 v[66:69], v[122:125], v[220:223], v[66:69]
	s_waitcnt lgkmcnt(5)
	v_mfma_f32_16x16x32_f16 v[78:81], v[122:125], v[224:227], v[78:81]
	s_waitcnt lgkmcnt(4)
	v_mfma_f32_16x16x32_f16 v[70:73], v[122:125], v[228:231], v[70:73]
	s_waitcnt vmcnt(13)
	v_mfma_f32_16x16x32_f16 v[54:57], v[156:159], v[176:179], v[54:57]
	v_mfma_f32_16x16x32_f16 v[74:77], v[156:159], v[220:223], v[74:77]
	v_mfma_f32_16x16x32_f16 v[82:85], v[156:159], v[224:227], v[82:85]
	v_mfma_f32_16x16x32_f16 v[62:65], v[156:159], v[228:231], v[62:65]
	s_waitcnt vmcnt(12)
	v_mfma_f32_16x16x32_f16 v[38:41], v[180:183], v[176:179], v[38:41]
	v_mfma_f32_16x16x32_f16 v[42:45], v[180:183], v[220:223], v[42:45]
	buffer_load_dwordx4 v[122:125], v147, s[16:19], s8 offen
	buffer_load_dwordx4 v[156:159], v148, s[16:19], s8 offen
	buffer_load_dwordx4 v[176:179], v149, s[16:19], s8 offen
	buffer_load_dwordx4 v[220:223], v150, s[16:19], s8 offen
	v_mfma_f32_16x16x32_f16 v[50:53], v[94:97], v[228:231], v[50:53]
	v_mfma_f32_16x16x32_f16 v[46:49], v[180:183], v[224:227], v[46:49]
	v_mfma_f32_16x16x32_f16 v[34:37], v[180:183], v[228:231], v[34:37]
	v_mfma_f32_16x16x32_f16 v[172:175], v[94:97], v[224:227], v[172:175]
	v_add_u32_e32 v98, s77, v98
	ds_read_b128 v[94:97], v98
	ds_read_b128 v[180:183], v98 offset:16384
	ds_read_b128 v[224:227], v98 offset:32768
	ds_read_b128 v[228:231], v98 offset:49152
	s_add_i32 s8, s22, s46
	s_waitcnt vmcnt(15) lgkmcnt(7)
	v_mfma_f32_16x16x32_f16 v[164:167], v[90:93], v[204:207], v[164:167]
	s_waitcnt lgkmcnt(6)
	v_mfma_f32_16x16x32_f16 v[168:171], v[90:93], v[208:211], v[168:171]
	s_waitcnt lgkmcnt(5)
	v_mfma_f32_16x16x32_f16 v[172:175], v[90:93], v[212:215], v[172:175]
	s_waitcnt lgkmcnt(4)
	v_mfma_f32_16x16x32_f16 v[90:93], v[90:93], v[216:219], v[50:53]
	s_waitcnt vmcnt(14)
	v_mfma_f32_16x16x32_f16 v[232:235], v[188:191], v[204:207], v[58:61]
	v_mfma_f32_16x16x32_f16 v[66:69], v[188:191], v[208:211], v[66:69]
	v_mfma_f32_16x16x32_f16 v[78:81], v[188:191], v[212:215], v[78:81]
	v_mfma_f32_16x16x32_f16 v[70:73], v[188:191], v[216:219], v[70:73]
	s_waitcnt vmcnt(13)
	v_mfma_f32_16x16x32_f16 v[188:191], v[192:195], v[204:207], v[54:57]
	v_mfma_f32_16x16x32_f16 v[74:77], v[192:195], v[208:211], v[74:77]
	v_mfma_f32_16x16x32_f16 v[82:85], v[192:195], v[212:215], v[82:85]
	v_mfma_f32_16x16x32_f16 v[62:65], v[192:195], v[216:219], v[62:65]
	s_waitcnt vmcnt(12)
	v_mfma_f32_16x16x32_f16 v[192:195], v[196:199], v[204:207], v[38:41]
	buffer_load_dwordx4 v[58:61], v147, s[16:19], s8 offen
	buffer_load_dwordx4 v[54:57], v148, s[16:19], s8 offen
	buffer_load_dwordx4 v[50:53], v149, s[16:19], s8 offen
	buffer_load_dwordx4 v[38:41], v150, s[16:19], s8 offen
	v_mfma_f32_16x16x32_f16 v[42:45], v[196:199], v[208:211], v[42:45]
	v_mfma_f32_16x16x32_f16 v[46:49], v[196:199], v[212:215], v[46:49]
	v_mfma_f32_16x16x32_f16 v[196:199], v[196:199], v[216:219], v[34:37]
	v_add_u32_e32 v99, s78, v99
	ds_read_b128 v[204:207], v99
	ds_read_b128 v[208:211], v99 offset:16384
	ds_read_b128 v[212:215], v99 offset:32768
	ds_read_b128 v[216:219], v99 offset:49152
	s_add_i32 s8, s22, s47
	s_waitcnt vmcnt(15) lgkmcnt(7)
	v_mfma_f32_16x16x32_f16 v[164:167], v[86:89], v[94:97], v[164:167]
	s_waitcnt lgkmcnt(6)
	v_mfma_f32_16x16x32_f16 v[168:171], v[86:89], v[180:183], v[168:171]
	s_waitcnt lgkmcnt(5)
	v_mfma_f32_16x16x32_f16 v[172:175], v[86:89], v[224:227], v[172:175]
	s_waitcnt lgkmcnt(4)
	v_mfma_f32_16x16x32_f16 v[86:89], v[86:89], v[228:231], v[90:93]
	s_waitcnt vmcnt(14)
	v_mfma_f32_16x16x32_f16 v[232:235], v[140:143], v[94:97], v[232:235]
	v_mfma_f32_16x16x32_f16 v[66:69], v[140:143], v[180:183], v[66:69]
	v_mfma_f32_16x16x32_f16 v[236:239], v[140:143], v[224:227], v[78:81]
	v_mfma_f32_16x16x32_f16 v[70:73], v[140:143], v[228:231], v[70:73]
	s_waitcnt vmcnt(13)
	v_mfma_f32_16x16x32_f16 v[140:143], v[152:155], v[94:97], v[188:191]
	v_mfma_f32_16x16x32_f16 v[74:77], v[152:155], v[180:183], v[74:77]
	v_mfma_f32_16x16x32_f16 v[82:85], v[152:155], v[224:227], v[82:85]
	v_mfma_f32_16x16x32_f16 v[62:65], v[152:155], v[228:231], v[62:65]
	s_waitcnt vmcnt(12)
	v_mfma_f32_16x16x32_f16 v[152:155], v[160:163], v[94:97], v[192:195]
	buffer_load_dwordx4 v[94:97], v147, s[16:19], s8 offen
	buffer_load_dwordx4 v[90:93], v148, s[16:19], s8 offen
	buffer_load_dwordx4 v[78:81], v149, s[16:19], s8 offen
	buffer_load_dwordx4 v[34:37], v150, s[16:19], s8 offen
	v_mfma_f32_16x16x32_f16 v[42:45], v[160:163], v[180:183], v[42:45]
	v_mfma_f32_16x16x32_f16 v[46:49], v[160:163], v[224:227], v[46:49]
	v_mfma_f32_16x16x32_f16 v[160:163], v[160:163], v[228:231], v[196:199]
	v_add_u32_e32 v100, s79, v100
	ds_read_b128 v[180:183], v100
	ds_read_b128 v[188:191], v100 offset:16384
	ds_read_b128 v[192:195], v100 offset:32768
	ds_read_b128 v[196:199], v100 offset:49152
	s_add_i32 s8, s22, s48
	s_waitcnt vmcnt(15) lgkmcnt(7)
	v_mfma_f32_16x16x32_f16 v[164:167], v[126:129], v[204:207], v[164:167]
	s_waitcnt lgkmcnt(6)
	v_mfma_f32_16x16x32_f16 v[168:171], v[126:129], v[208:211], v[168:171]
	s_waitcnt lgkmcnt(5)
	v_mfma_f32_16x16x32_f16 v[172:175], v[126:129], v[212:215], v[172:175]
	s_waitcnt lgkmcnt(4)
	v_mfma_f32_16x16x32_f16 v[86:89], v[126:129], v[216:219], v[86:89]
	s_waitcnt vmcnt(14)
	v_mfma_f32_16x16x32_f16 v[126:129], v[136:139], v[204:207], v[232:235]
	v_mfma_f32_16x16x32_f16 v[66:69], v[136:139], v[208:211], v[66:69]
	v_mfma_f32_16x16x32_f16 v[224:227], v[136:139], v[212:215], v[236:239]
	v_mfma_f32_16x16x32_f16 v[136:139], v[136:139], v[216:219], v[70:73]
	s_waitcnt vmcnt(13)
	v_mfma_f32_16x16x32_f16 v[140:143], v[184:187], v[204:207], v[140:143]
	v_mfma_f32_16x16x32_f16 v[74:77], v[184:187], v[208:211], v[74:77]
	v_mfma_f32_16x16x32_f16 v[228:231], v[184:187], v[212:215], v[82:85]
	v_mfma_f32_16x16x32_f16 v[184:187], v[184:187], v[216:219], v[62:65]
	s_waitcnt vmcnt(12)
	v_mfma_f32_16x16x32_f16 v[152:155], v[200:203], v[204:207], v[152:155]
	v_mfma_f32_16x16x32_f16 v[204:207], v[200:203], v[208:211], v[42:45]
	buffer_load_dwordx4 v[82:85], v147, s[16:19], s8 offen
	buffer_load_dwordx4 v[70:73], v148, s[16:19], s8 offen
	buffer_load_dwordx4 v[62:65], v149, s[16:19], s8 offen
	buffer_load_dwordx4 v[42:45], v150, s[16:19], s8 offen
	v_mfma_f32_16x16x32_f16 v[46:49], v[200:203], v[212:215], v[46:49]
	v_mfma_f32_16x16x32_f16 v[160:163], v[200:203], v[216:219], v[160:163]
	v_add_u32_e32 v0, 0x1ac00, v104
	ds_read_b128 v[240:243], v0
	ds_read_b128 v[244:247], v0 offset:16
	s_waitcnt vmcnt(12) lgkmcnt(5)
	v_mfma_f32_16x16x32_f16 v[164:167], v[122:125], v[180:183], v[164:167]
	v_mfma_f32_16x16x32_f16 v[126:129], v[156:159], v[180:183], v[126:129]
	v_mfma_f32_16x16x32_f16 v[140:143], v[176:179], v[180:183], v[140:143]
	v_mfma_f32_16x16x32_f16 v[152:155], v[220:223], v[180:183], v[152:155]
	s_waitcnt lgkmcnt(4)
	v_mfma_f32_16x16x32_f16 v[168:171], v[122:125], v[188:191], v[168:171]
	v_mfma_f32_16x16x32_f16 v[208:211], v[156:159], v[188:191], v[66:69]
	v_mfma_f32_16x16x32_f16 v[212:215], v[176:179], v[188:191], v[74:77]
	v_mfma_f32_16x16x32_f16 v[204:207], v[220:223], v[188:191], v[204:207]
	s_waitcnt lgkmcnt(3)
	v_mfma_f32_16x16x32_f16 v[172:175], v[122:125], v[192:195], v[172:175]
	v_cvt_pk_f16_f32 v232, v164, v165
	v_cvt_pk_f16_f32 v233, v166, v167
	v_pk_max_f16 v232, v232, 0
	v_pk_max_f16 v233, v233, 0
	v_mfma_f32_16x16x32_f16 v[224:227], v[156:159], v[192:195], v[224:227]
	v_cvt_pk_f16_f32 v234, v126, v127
	v_cvt_pk_f16_f32 v235, v128, v129
	v_pk_max_f16 v234, v234, 0
	v_pk_max_f16 v235, v235, 0
	v_mfma_f32_16x16x32_f16 v[228:231], v[176:179], v[192:195], v[228:231]
	v_cvt_pk_f16_f32 v236, v140, v141
	v_cvt_pk_f16_f32 v237, v142, v143
	v_pk_max_f16 v236, v236, 0
	v_pk_max_f16 v237, v237, 0
	v_mfma_f32_16x16x32_f16 v[216:219], v[220:223], v[192:195], v[46:49]
	v_cvt_pk_f16_f32 v238, v152, v153
	v_cvt_pk_f16_f32 v239, v154, v155
	v_pk_max_f16 v238, v238, 0
	v_pk_max_f16 v239, v239, 0
	s_waitcnt lgkmcnt(2)
	v_mfma_f32_16x16x32_f16 v[200:203], v[122:125], v[196:199], v[86:89]
	v_cvt_pk_f16_f32 v180, v168, v169
	v_cvt_pk_f16_f32 v181, v170, v171
	v_pk_max_f16 v180, v180, 0
	v_pk_max_f16 v181, v181, 0
	s_add_i32 s8, s22, s49
	buffer_load_dwordx4 v[86:89], v147, s[16:19], s8 offen
	buffer_load_dwordx4 v[74:77], v148, s[16:19], s8 offen
	buffer_load_dwordx4 v[66:69], v149, s[16:19], s8 offen
	buffer_load_dwordx4 v[46:49], v150, s[16:19], s8 offen
	v_mfma_f32_16x16x32_f16 v[136:139], v[156:159], v[196:199], v[136:139]
	v_cvt_pk_f16_f32 v182, v208, v209
	v_cvt_pk_f16_f32 v183, v210, v211
	v_pk_max_f16 v182, v182, 0
	v_pk_max_f16 v183, v183, 0
	s_waitcnt lgkmcnt(1)
	v_mfma_f32_16x16x32_f16 v[252:255], v[240:243], v[232:235], 0
	v_cvt_pk_f16_f32 v232, v172, v173
	v_cvt_pk_f16_f32 v233, v174, v175
	v_pk_max_f16 v232, v232, 0
	v_pk_max_f16 v233, v233, 0
	v_mfma_f32_16x16x32_f16 v[184:187], v[176:179], v[196:199], v[184:187]
	v_cvt_pk_f16_f32 v188, v212, v213
	v_cvt_pk_f16_f32 v189, v214, v215
	v_pk_max_f16 v188, v188, 0
	v_pk_max_f16 v189, v189, 0
	s_waitcnt lgkmcnt(0)
	v_mfma_f32_16x16x32_f16 v[252:255], v[244:247], v[236:239], v[252:255]
	ds_read_u16 v102, v114
	ds_read_u16 v103, v114 offset:512
	ds_read_u16 v115, v114 offset:1024
	ds_read_u16 v116, v114 offset:1536
	v_cvt_pk_f16_f32 v234, v224, v225
	v_cvt_pk_f16_f32 v235, v226, v227
	v_pk_max_f16 v234, v234, 0
	v_pk_max_f16 v235, v235, 0
	v_mfma_f32_16x16x32_f16 v[160:163], v[220:223], v[196:199], v[160:163]
	v_cvt_pk_f16_f32 v190, v204, v205
	v_cvt_pk_f16_f32 v191, v206, v207
	v_pk_max_f16 v190, v190, 0
	v_pk_max_f16 v191, v191, 0
	v_mfma_f32_16x16x32_f16 v[192:195], v[240:243], v[180:183], 0
	v_cvt_pk_f16_f32 v236, v228, v229
	v_cvt_pk_f16_f32 v237, v230, v231
	v_pk_max_f16 v236, v236, 0
	v_pk_max_f16 v237, v237, 0
	v_mfma_f32_16x16x32_f16 v[192:195], v[244:247], v[188:191], v[192:195]
	v_cvt_pk_f16_f32 v238, v216, v217
	v_cvt_pk_f16_f32 v239, v218, v219
	v_pk_max_f16 v238, v238, 0
	v_pk_max_f16 v239, v239, 0
	v_cvt_pk_f16_f32 v180, v200, v201
	v_cvt_pk_f16_f32 v181, v202, v203
	v_pk_max_f16 v180, v180, 0
	v_pk_max_f16 v181, v181, 0
	v_mfma_f32_16x16x32_f16 v[196:199], v[240:243], v[232:235], 0
	v_cvt_pk_f16_f32 v182, v136, v137
	v_cvt_pk_f16_f32 v183, v138, v139
	v_pk_max_f16 v182, v182, 0
	v_pk_max_f16 v183, v183, 0
	v_mfma_f32_16x16x32_f16 v[196:199], v[244:247], v[236:239], v[196:199]
	v_cvt_pk_f16_f32 v188, v184, v185
	v_cvt_pk_f16_f32 v189, v186, v187
	v_pk_max_f16 v188, v188, 0
	v_pk_max_f16 v189, v189, 0
	v_cvt_pk_f16_f32 v190, v160, v161
	v_cvt_pk_f16_f32 v191, v162, v163
	v_pk_max_f16 v190, v190, 0
	v_pk_max_f16 v191, v191, 0
	v_mfma_f32_16x16x32_f16 v[122:125], v[240:243], v[180:183], 0
	s_nop 0
	v_mfma_f32_16x16x32_f16 v[122:125], v[244:247], v[188:191], v[122:125]
	v_add_u32_e32 v145, 0x12c00, v105
	ds_read_b128 v[240:243], v145 offset:2048
	ds_read_b128 v[244:247], v145 offset:2064
	ds_read_b128 v[248:251], v145 offset:2080
	s_load_dword s30, s[12:13], 0x0
	v_cndmask_b32_e64 v0, v252, v192, s[2:3]
	ds_read_b128 v[252:255], v145 offset:2096
	v_cndmask_b32_e64 v0, v0, v196, s[0:1]
	v_cndmask_b32_e64 v0, v0, v122, s[26:27]
	ds_write_b32 v112, v0
	s_waitcnt vmcnt(16)
	v_cndmask_b32_e64 v1, v30, v134, s[0:1]
	v_bfi_b32 v30, s10, v1, v30
	v_perm_b32 v1, v22, v134, s24
	v_cndmask_b32_e64 v22, v22, v1, s[0:1]
	v_bfi_b32 v1, s10, v135, v18
	v_perm_b32 v121, v10, v135, s24
	v_cndmask_b32_e64 v18, v18, v1, s[0:1]
	v_cndmask_b32_e64 v10, v10, v121, s[0:1]
	s_add_i32 s22, s22, 0x80000
	s_add_i32 s11, s11, 1
	s_add_u32 s12, s12, 4
	s_addc_u32 s13, s13, 0
	v_add_u32_e32 v104, 0x400, v104
	v_add_u32_e32 v105, 0x800, v105
	v_add_u32_e32 v114, 2, v114
	s_cmp_eq_u32 s22, 0x898000
	s_waitcnt lgkmcnt(0)
	s_barrier
	ds_read_b128 v[232:235], v113
	ds_read_b128 v[236:239], v113 offset:1024
	s_waitcnt lgkmcnt(0)
	v_add_f32_e32 v0, v232, v233
	v_add_f32_e32 v1, v234, v235
	v_add_f32_e32 v121, v236, v237
	v_add_f32_e32 v144, v238, v239
	v_add_f32_e32 v0, v0, v1
	v_add_f32_e32 v121, v121, v144
	v_add_f32_e32 v0, v0, v121
	v_add_f32_e32 v0, s30, v0
	ds_write_b32 v106, v0
	v_cvt_f16_f32_e32 v1, v0
	v_cvt_f16_f32_e32 v121, v0
	s_nop 1
	v_permlane16_swap_b32_e32 v1, v121
	v_mov_b32_e32 v144, v1
	v_mov_b32_e32 v145, v121
	s_nop 1
	v_permlane32_swap_b32_e32 v1, v144
	v_permlane32_swap_b32_e32 v121, v145
	v_add_u32_e32 v106, 4, v106
	s_cbranch_scc0 .LBB1_4
